# hand-written 4-buffer ring main loop (3 tiles in flight) and nt cache policy on the per-tile mask loads
# speedup vs baseline: 1.0238x; 1.0126x over previous
_Z10k_attn_epiILi2EEvPKfS1_PKiPKDF16_S5_PfS1_S1_S5_S1_S1_S1_S1_S1_S6_:
	s_load_dwordx8 s[12:19], s[0:1], 0x0
	s_load_dwordx2 s[4:5], s[0:1], 0x20
	s_load_dwordx4 s[20:23], s[0:1], 0x30
	v_and_b32_e32 v196, 63, v0
	v_cmp_gt_u32_e64 s[6:7], 32, v196
	s_waitcnt lgkmcnt(0)
	v_mov_b32_e32 v1, s15
	v_mov_b32_e32 v2, s13
	v_lshrrev_b32_e32 v197, 6, v0
	s_lshl_b32 s31, s2, 3
	v_cndmask_b32_e64 v103, v1, v2, s[6:7]
	v_mov_b32_e32 v1, s14
	v_mov_b32_e32 v2, s12
	v_or_b32_e32 v104, s31, v197
	v_cndmask_b32_e64 v102, v1, v2, s[6:7]
	s_mov_b32 s8, 0x19000
	v_lshlrev_b32_e32 v1, 4, v0
	v_mad_i64_i32 v[2:3], s[2:3], v104, s8, v[102:103]
	v_and_b32_e32 v108, 0x1f0, v1
	v_mov_b32_e32 v109, 0
	v_lshl_add_u64 v[14:15], v[2:3], 0, v[108:109]
	v_mov_b32_e32 v2, s23
	v_mov_b32_e32 v3, s21
	v_ashrrev_i32_e32 v105, 31, v104
	v_cndmask_b32_e64 v3, v2, v3, s[6:7]
	v_mov_b32_e32 v2, s22
	v_mov_b32_e32 v4, s20
	v_cndmask_b32_e64 v2, v2, v4, s[6:7]
	v_lshlrev_b64 v[4:5], 9, v[104:105]
	v_lshl_add_u64 v[2:3], v[2:3], 0, v[4:5]
	v_lshlrev_b32_e32 v122, 10, v197
	v_lshl_add_u64 v[2:3], v[2:3], 0, v[108:109]
	v_or_b32_e32 v106, v122, v196
	global_load_dwordx4 v[82:85], v[2:3], off
	v_lshlrev_b32_e32 v2, 4, v106
	v_or_b32_e32 v123, 0x100, v122
	global_load_dwordx4 v[86:89], v2, s[18:19]
	global_load_dwordx4 v[90:93], v2, s[18:19] offset:1024
	global_load_dwordx4 v[94:97], v2, s[18:19] offset:2048
	global_load_dwordx4 v[98:101], v2, s[18:19] offset:3072
	v_or_b32_e32 v2, v123, v196
	v_or_b32_e32 v124, 0x140, v122
	v_lshlrev_b32_e32 v131, 4, v2
	v_or_b32_e32 v2, v124, v196
	v_or_b32_e32 v125, 0x180, v122
	v_lshlrev_b32_e32 v132, 4, v2
	v_or_b32_e32 v2, v125, v196
	v_or_b32_e32 v126, 0x1c0, v122
	v_lshlrev_b32_e32 v133, 4, v2
	v_or_b32_e32 v2, v126, v196
	v_or_b32_e32 v127, 0x200, v122
	v_lshlrev_b32_e32 v134, 4, v2
	v_or_b32_e32 v2, v127, v196
	v_or_b32_e32 v128, 0x240, v122
	v_lshlrev_b32_e32 v135, 4, v2
	v_or_b32_e32 v2, v128, v196
	v_or_b32_e32 v129, 0x280, v122
	v_lshlrev_b32_e32 v137, 4, v2
	v_or_b32_e32 v2, v129, v196
	v_or_b32_e32 v130, 0x2c0, v122
	v_lshlrev_b32_e32 v136, 4, v2
	v_or_b32_e32 v2, v130, v196
	v_or_b32_e32 v192, 0x300, v122
	v_lshlrev_b32_e32 v142, 4, v2
	v_or_b32_e32 v2, v192, v196
	v_or_b32_e32 v202, 0x340, v122
	v_lshlrev_b32_e32 v143, 4, v2
	v_or_b32_e32 v2, v202, v196
	v_or_b32_e32 v203, 0x380, v122
	v_lshlrev_b32_e32 v144, 4, v2
	v_or_b32_e32 v2, v203, v196
	v_or_b32_e32 v204, 0x3c0, v122
	s_movk_i32 s2, 0xc8
	v_bfe_u32 v1, v0, 3, 3
	v_lshlrev_b32_e32 v145, 4, v2
	v_or_b32_e32 v2, v204, v196
	v_mad_i64_i32 v[182:183], s[2:3], v104, s2, 0
	v_lshlrev_b32_e32 v150, 4, v2
	v_lshl_add_u64 v[2:3], v[182:183], 2, s[16:17]
	v_lshlrev_b32_e32 v108, 2, v1
	v_lshlrev_b32_e32 v1, 9, v197
	v_lshl_add_u64 v[16:17], v[2:3], 0, v[108:109]
	v_or_b32_e32 v3, v1, v196
	v_or_b32_e32 v2, 0x100, v1
	v_lshlrev_b32_e32 v3, 4, v3
	global_load_dwordx4 v[110:113], v131, s[18:19]
	global_load_dwordx4 v[114:117], v132, s[18:19]
	global_load_dwordx4 v[118:121], v133, s[18:19]
	global_load_dwordx4 v[138:141], v134, s[18:19]
	global_load_dwordx4 v[146:149], v135, s[18:19]
	global_load_dwordx4 v[152:155], v137, s[18:19]
	global_load_dwordx4 v[156:159], v136, s[18:19]
	global_load_dwordx4 v[160:163], v142, s[18:19]
	global_load_dwordx4 v[164:167], v143, s[18:19]
	global_load_dwordx4 v[168:171], v144, s[18:19]
	global_load_dwordx4 v[172:175], v145, s[18:19]
	global_load_dwordx4 v[176:179], v150, s[18:19]
	global_load_dwordx4 v[186:189], v3, s[4:5]
	global_load_dwordx4 v[206:209], v3, s[4:5] offset:1024
	global_load_dwordx4 v[210:213], v3, s[4:5] offset:2048
	global_load_dwordx4 v[214:217], v3, s[4:5] offset:3072
	v_or_b32_e32 v3, v2, v196
	v_or_b32_e32 v4, 0x140, v1
	v_lshlrev_b32_e32 v3, 4, v3
	v_or_b32_e32 v5, v4, v196
	v_or_b32_e32 v10, 0x180, v1
	v_or_b32_e32 v12, 0x1000, v196
	v_lshlrev_b32_e32 v5, 4, v5
	global_load_dwordx4 v[42:45], v3, s[4:5]
	global_load_dwordx4 v[50:53], v5, s[4:5]
	v_or_b32_e32 v3, v10, v196
	v_or_b32_e32 v11, 0x1c0, v1
	v_or_b32_e32 v1, v1, v12
	v_lshlrev_b32_e32 v3, 4, v3
	v_or_b32_e32 v5, v11, v196
	v_lshlrev_b32_e32 v1, 4, v1
	v_lshlrev_b32_e32 v5, 4, v5
	global_load_dwordx4 v[78:81], v3, s[4:5]
	global_load_dwordx4 v[74:77], v5, s[4:5]
	global_load_dwordx4 v[38:41], v1, s[4:5]
	global_load_dwordx4 v[30:33], v1, s[4:5] offset:1024
	global_load_dwordx4 v[22:25], v1, s[4:5] offset:2048
	global_load_dwordx4 v[26:29], v1, s[4:5] offset:3072
	v_or_b32_e32 v1, v2, v12
	v_or_b32_e32 v2, v4, v12
	v_lshlrev_b32_e32 v1, 4, v1
	v_lshlrev_b32_e32 v6, 4, v2
	global_load_dwordx4 v[2:5], v1, s[4:5]
	s_nop 0
	global_load_dwordx4 v[6:9], v6, s[4:5]
	v_or_b32_e32 v1, v10, v12
	v_or_b32_e32 v10, v11, v12
	v_lshlrev_b32_e32 v1, 4, v1
	v_lshlrev_b32_e32 v10, 4, v10
	global_load_dwordx4 v[18:21], v1, s[4:5]
	s_nop 0
	global_load_dwordx4 v[10:13], v10, s[4:5]
	s_nop 0
	global_load_dword v107, v[16:17], off nt
	global_load_dwordx4 v[70:73], v[14:15], off nt
	global_load_dwordx4 v[66:69], v[14:15], off offset:512 nt
	global_load_dwordx4 v[62:65], v[14:15], off offset:1024 nt
	global_load_dwordx4 v[58:61], v[14:15], off offset:1536 nt
	global_load_dwordx4 v[54:57], v[14:15], off offset:2048 nt
	global_load_dwordx4 v[46:49], v[14:15], off offset:2560 nt
	global_load_dwordx4 v[34:37], v[14:15], off offset:3072 nt
	s_nop 0
	global_load_dwordx4 v[14:17], v[14:15], off offset:3584 nt
	v_bfe_u32 v195, v0, 4, 2
	v_and_b32_e32 v1, 15, v0
	s_waitcnt vmcnt(41)
	v_cvt_pk_f16_f32 v85, v84, v85
	v_cvt_pk_f16_f32 v84, v82, v83
	v_lshlrev_b32_e32 v82, 3, v196
	s_movk_i32 s2, 0x410
	v_mad_u32_u24 v185, v197, s2, v82
	v_and_b32_e32 v82, 7, v0
	v_and_b32_e32 v194, 48, v0
	v_mad_u32_u24 v105, v82, s2, v194
	ds_write_b64 v185, v[84:85]
	s_waitcnt lgkmcnt(0)
	s_barrier
	ds_read_b128 v[82:85], v105
	ds_read_b128 v[198:201], v105 offset:64
	s_waitcnt vmcnt(40) lgkmcnt(1)
	v_mfma_f32_16x16x32_f16 v[86:89], v[82:85], v[86:89], 0
	s_movk_i32 s2, 0x840
	s_waitcnt vmcnt(32)
	v_mfma_f32_16x16x32_f16 v[82:85], v[82:85], v[146:149], 0
	s_waitcnt lgkmcnt(0)
	v_mfma_f32_16x16x32_f16 v[86:89], v[198:201], v[90:93], v[86:89]
	ds_read_b128 v[90:93], v105 offset:128
	ds_read_b128 v[146:149], v105 offset:192
	s_waitcnt vmcnt(31)
	v_mfma_f32_16x16x32_f16 v[82:85], v[198:201], v[152:155], v[82:85]
	v_lshlrev_b32_e32 v200, 7, v197
	v_lshl_or_b32 v109, v1, 2, v200
	v_add_u32_e32 v109, 0x4100, v109
	s_waitcnt lgkmcnt(1)
	v_mfma_f32_16x16x32_f16 v[86:89], v[90:93], v[94:97], v[86:89]
	ds_read_b128 v[94:97], v105 offset:320
	v_lshl_add_u32 v109, v195, 13, v109
	s_waitcnt vmcnt(30)
	v_mfma_f32_16x16x32_f16 v[82:85], v[90:93], v[156:159], v[82:85]
	ds_read_b128 v[90:93], v105 offset:256
	s_waitcnt lgkmcnt(2)
	v_mfma_f32_16x16x32_f16 v[86:89], v[146:149], v[98:101], v[86:89]
	ds_read_b128 v[98:101], v105 offset:384
	s_waitcnt vmcnt(29)
	v_mfma_f32_16x16x32_f16 v[82:85], v[146:149], v[160:163], v[82:85]
	s_waitcnt lgkmcnt(1)
	v_mfma_f32_16x16x32_f16 v[86:89], v[90:93], v[110:113], v[86:89]
	ds_read_b128 v[110:113], v105 offset:448
	v_and_b32_e32 v105, 0x1c0, v0
	v_mfma_f32_16x16x32_f16 v[86:89], v[94:97], v[114:117], v[86:89]
	s_waitcnt vmcnt(28)
	v_mfma_f32_16x16x32_f16 v[82:85], v[90:93], v[164:167], v[82:85]
	v_mad_u32_u24 v90, v195, s2, v105
	v_lshl_or_b32 v105, v1, 1, v90
	s_movk_i32 s2, 0x210
	s_waitcnt lgkmcnt(1)
	v_mfma_f32_16x16x32_f16 v[86:89], v[98:101], v[118:121], v[86:89]
	s_waitcnt vmcnt(27)
	v_mfma_f32_16x16x32_f16 v[82:85], v[94:97], v[168:171], v[82:85]
	s_waitcnt lgkmcnt(0)
	v_mfma_f32_16x16x32_f16 v[86:89], v[110:113], v[138:141], v[86:89]
	s_waitcnt vmcnt(26)
	v_mfma_f32_16x16x32_f16 v[82:85], v[98:101], v[172:175], v[82:85]
	s_waitcnt vmcnt(25)
	v_mfma_f32_16x16x32_f16 v[82:85], v[110:113], v[176:179], v[82:85]
	s_nop 3
	v_cvt_f16_f32_e32 v86, v86
	ds_write_b16 v105, v86 offset:58624
	v_cvt_f16_f32_e32 v86, v87
	s_nop 0
	v_cvt_f16_f32_e32 v82, v82
	v_cvt_f16_f32_e32 v87, v88
	v_cvt_f16_f32_e32 v83, v83
	v_cvt_f16_f32_e32 v88, v89
	v_cvt_f16_f32_e32 v84, v84
	v_cvt_f16_f32_e32 v85, v85
	ds_write_b16 v105, v86 offset:59152
	ds_write_b16 v105, v87 offset:59680
	ds_write_b16 v105, v88 offset:60208
	ds_write_b16 v105, v82 offset:58656
	ds_write_b16 v105, v83 offset:59184
	ds_write_b16 v105, v84 offset:59712
	ds_write_b16 v105, v85 offset:60240
	v_mov_b32_e32 v82, 0xe500
	v_mad_u32_u24 v82, v1, s2, v82
	v_add_u32_e32 v198, v82, v194
	s_waitcnt lgkmcnt(0)
	s_barrier
	ds_read_b128 v[82:85], v198
	ds_read_b128 v[86:89], v198 offset:64
	s_waitcnt vmcnt(24) lgkmcnt(1)
	v_mfma_f32_16x16x32_f16 v[94:97], v[82:85], v[186:189], 0
	ds_read_b128 v[90:93], v198 offset:128
	s_waitcnt vmcnt(23) lgkmcnt(1)
	v_mfma_f32_16x16x32_f16 v[98:101], v[86:89], v[206:209], v[94:97]
	s_nop 4
	ds_read_b128 v[94:97], v198 offset:192
	s_waitcnt vmcnt(22) lgkmcnt(1)
	v_mfma_f32_16x16x32_f16 v[98:101], v[90:93], v[210:213], v[98:101]
	s_waitcnt vmcnt(21) lgkmcnt(0)
	v_mfma_f32_16x16x32_f16 v[98:101], v[94:97], v[214:217], v[98:101]
	s_and_saveexec_b64 s[2:3], s[6:7]
	s_cbranch_execz .LBB1_2
	s_nop 5
	v_mul_f32_e32 v98, 0x3e0293ee, v98
	v_mul_f32_e32 v99, 0x3e0293ee, v99
	ds_write2st64_b32 v109, v98, v99 offset1:8
	v_mul_f32_e32 v98, 0x3e0293ee, v100
	v_mul_f32_e32 v99, 0x3e0293ee, v101
	ds_write2st64_b32 v109, v98, v99 offset0:16 offset1:24

.LBB1_8:
	s_or_b64 exec, exec, s[2:3]
	s_nop 4
	v_lshlrev_b32_e32 v2, 11, v197
	v_lshl_or_b32 v2, v184, 2, v2
	s_waitcnt lgkmcnt(0)
	s_barrier
	ds_read_b128 v[10:13], v2 offset:16640
	ds_read_b128 v[6:9], v2 offset:17664
	v_and_b32_e32 v2, 8, v0
	v_cmp_eq_u32_e64 s[4:5], 0, v2
	v_and_b32_e32 v2, 4, v0
	s_load_dwordx2 s[18:19], s[0:1], 0x70
	v_cmp_eq_u32_e64 s[2:3], 0, v2
	v_and_b32_e32 v2, 3, v0
	s_movk_i32 s0, 0x320
	v_cmp_eq_u32_e32 vcc, 0, v2
	v_mad_i64_i32 v[2:3], s[0:1], v104, s0, 0
	v_or_b32_e32 v2, v2, v108
	v_bfe_u32 v109, v0, 2, 1
	v_lshl_add_u64 v[2:3], s[16:17], 0, v[2:3]
	v_lshl_add_u64 v[254:255], v[2:3], 0, 32
	v_mul_u32_u24_e32 v2, 0x320, v109
	s_movk_i32 s0, 0x640
	v_mad_u32_u24 v2, v197, s0, v2
	v_and_b32_e32 v199, 31, v0
	v_or_b32_e32 v2, v2, v108
	v_lshlrev_b32_e32 v186, 4, v199
	v_mov_b32_e32 v187, 0
	v_add_u32_e32 v251, 0x8200, v2
	v_lshl_add_u64 v[2:3], v[78:79], 0, v[186:187]
	v_lshl_add_u64 v[2:3], v[102:103], 0, v[2:3]
	s_mov_b64 s[0:1], 0x1000
	v_add_u32_e32 v201, 0xe500, v105
	v_lshl_add_u64 v[252:253], v[2:3], 0, s[0:1]
	v_mov_b32_e32 v248, 0xff800000
	v_mov_b32_e32 v250, 0xd01502f9
	s_mov_b64 s[16:17], 0x1000
	v_mov_b32_e32 v240, 0
	v_mov_b32_e32 v241, 0
	v_mov_b32_e32 v242, 0
	v_mov_b32_e32 v243, 0
	v_mov_b32_e32 v244, 0
	v_mov_b32_e32 v245, 0
	v_mov_b32_e32 v246, 0
	v_mov_b32_e32 v247, 0
	v_mov_b32_e32 v249, 0
	s_mov_b32 s30, 0
	global_load_dword v110, v[254:255], off nt
	global_load_dwordx4 v[102:105], v[252:253], off nt
	global_load_dwordx4 v[98:101], v[252:253], off offset:512 nt
	global_load_dwordx4 v[94:97], v[252:253], off offset:1024 nt
	global_load_dwordx4 v[90:93], v[252:253], off offset:1536 nt
	global_load_dwordx4 v[86:89], v[252:253], off offset:2048 nt
	global_load_dwordx4 v[82:85], v[252:253], off offset:2560 nt
	global_load_dwordx4 v[78:81], v[252:253], off offset:3072 nt
	global_load_dwordx4 v[74:77], v[252:253], off offset:3584 nt
	v_lshl_add_u64 v[252:253], v[252:253], 0, s[16:17]
	v_lshl_add_u64 v[254:255], v[254:255], 0, 32
	global_load_dword v111, v[254:255], off nt
	global_load_dwordx4 v[50:53], v[252:253], off nt
	global_load_dwordx4 v[42:45], v[252:253], off offset:512 nt
	global_load_dwordx4 v[38:41], v[252:253], off offset:1024 nt
	global_load_dwordx4 v[30:33], v[252:253], off offset:1536 nt
	global_load_dwordx4 v[26:29], v[252:253], off offset:2048 nt
	global_load_dwordx4 v[22:25], v[252:253], off offset:2560 nt
	global_load_dwordx4 v[18:21], v[252:253], off offset:3072 nt
	global_load_dwordx4 v[2:5], v[252:253], off offset:3584 nt
	v_lshl_add_u64 v[252:253], v[252:253], 0, s[16:17]
	v_lshl_add_u64 v[254:255], v[254:255], 0, 32
	global_load_dword v112, v[254:255], off nt
	global_load_dwordx4 v[138:141], v[252:253], off nt
	global_load_dwordx4 v[146:149], v[252:253], off offset:512 nt
	global_load_dwordx4 v[152:155], v[252:253], off offset:1024 nt
	global_load_dwordx4 v[156:159], v[252:253], off offset:1536 nt
	global_load_dwordx4 v[160:163], v[252:253], off offset:2048 nt
	global_load_dwordx4 v[164:167], v[252:253], off offset:2560 nt
	global_load_dwordx4 v[168:171], v[252:253], off offset:3072 nt
	global_load_dwordx4 v[172:175], v[252:253], off offset:3584 nt
	v_lshl_add_u64 v[252:253], v[252:253], 0, s[16:17]
	v_lshl_add_u64 v[254:255], v[254:255], 0, 32
	s_waitcnt lgkmcnt(0)
.Lring_tile_0:
	s_cmp_lt_u32 s30, 22
	s_cbranch_scc1 .Lring_w27_0
	s_waitcnt vmcnt(0)
	s_branch .Lring_go_0
.Lring_w27_0:
	s_waitcnt vmcnt(27)
.Lring_go_0:
	v_mul_f32_e32 v205, v10, v70
	v_mul_f32_e32 v206, v6, v70
	v_mul_f32_e32 v207, v10, v66
	v_mul_f32_e32 v208, v6, v66
	v_mul_f32_e32 v209, v10, v62
	v_mul_f32_e32 v210, v6, v62
	v_mul_f32_e32 v211, v10, v58
	v_mul_f32_e32 v212, v6, v58
	v_mul_f32_e32 v213, v10, v54
	v_mul_f32_e32 v214, v6, v54
	v_mul_f32_e32 v215, v10, v46
	v_mul_f32_e32 v216, v6, v46
	v_mul_f32_e32 v217, v10, v34
	v_mul_f32_e32 v218, v6, v34
	v_mul_f32_e32 v219, v10, v14
	v_mul_f32_e32 v220, v6, v14
	v_fmac_f32_e32 v205, v71, v11
	v_fmac_f32_e32 v206, v71, v7
	v_fmac_f32_e32 v207, v67, v11
	v_fmac_f32_e32 v208, v67, v7
	v_fmac_f32_e32 v209, v63, v11
	v_fmac_f32_e32 v210, v63, v7
	v_fmac_f32_e32 v211, v59, v11
	v_fmac_f32_e32 v212, v59, v7
	v_fmac_f32_e32 v213, v55, v11
	v_fmac_f32_e32 v214, v55, v7
	v_fmac_f32_e32 v215, v47, v11
	v_fmac_f32_e32 v216, v47, v7
	v_fmac_f32_e32 v217, v35, v11
	v_fmac_f32_e32 v218, v35, v7
	v_fmac_f32_e32 v219, v15, v11
	v_fmac_f32_e32 v220, v15, v7
	v_fmac_f32_e32 v205, v72, v12
	v_fmac_f32_e32 v206, v72, v8
	v_fmac_f32_e32 v207, v68, v12
	v_fmac_f32_e32 v208, v68, v8
	v_fmac_f32_e32 v209, v64, v12
	v_fmac_f32_e32 v210, v64, v8
	v_fmac_f32_e32 v211, v60, v12
	v_fmac_f32_e32 v212, v60, v8
	v_fmac_f32_e32 v213, v56, v12
	v_fmac_f32_e32 v214, v56, v8
	v_fmac_f32_e32 v215, v48, v12
	v_fmac_f32_e32 v216, v48, v8
	v_fmac_f32_e32 v217, v36, v12
	v_fmac_f32_e32 v218, v36, v8
	v_fmac_f32_e32 v219, v16, v12
	v_fmac_f32_e32 v220, v16, v8
	v_fmac_f32_e32 v205, v73, v13
	v_fmac_f32_e32 v206, v73, v9
	v_fmac_f32_e32 v207, v69, v13
	v_fmac_f32_e32 v208, v69, v9
	v_fmac_f32_e32 v209, v65, v13
	v_fmac_f32_e32 v210, v65, v9
	v_fmac_f32_e32 v211, v61, v13
	v_fmac_f32_e32 v212, v61, v9
	v_fmac_f32_e32 v213, v57, v13
	v_fmac_f32_e32 v214, v57, v9
	v_fmac_f32_e32 v215, v49, v13
	v_fmac_f32_e32 v216, v49, v9
	v_fmac_f32_e32 v217, v37, v13
	v_fmac_f32_e32 v218, v37, v9
	v_fmac_f32_e32 v219, v17, v13
	v_fmac_f32_e32 v220, v17, v9
	v_permlane32_swap_b32_e32 v205, v213
	v_permlane32_swap_b32_e32 v206, v214
	v_permlane32_swap_b32_e32 v207, v215
	v_permlane32_swap_b32_e32 v208, v216
	v_permlane32_swap_b32_e32 v209, v217
	v_permlane32_swap_b32_e32 v210, v218
	v_permlane32_swap_b32_e32 v211, v219
	v_permlane32_swap_b32_e32 v212, v220
	v_add_f32_e32 v205, v205, v213
	v_add_f32_e32 v206, v206, v214
	v_add_f32_e32 v207, v207, v215
	v_add_f32_e32 v208, v208, v216
	v_add_f32_e32 v209, v209, v217
	v_add_f32_e32 v210, v210, v218
	v_add_f32_e32 v211, v211, v219
	v_add_f32_e32 v212, v212, v220
	v_permlane16_swap_b32_e32 v205, v209
	v_permlane16_swap_b32_e32 v206, v210
	v_permlane16_swap_b32_e32 v207, v211
	v_permlane16_swap_b32_e32 v208, v212
	v_add_f32_e32 v205, v205, v209
	v_add_f32_e32 v206, v206, v210
	v_add_f32_e32 v207, v207, v211
	v_add_f32_e32 v208, v208, v212
	v_add_f32_dpp v205, v205, v205 row_ror:8 row_mask:0xf bank_mask:0xf bound_ctrl:1
	v_add_f32_dpp v207, v207, v207 row_ror:8 row_mask:0xf bank_mask:0xf bound_ctrl:1
	v_add_f32_dpp v206, v206, v206 row_ror:8 row_mask:0xf bank_mask:0xf bound_ctrl:1
	v_add_f32_dpp v208, v208, v208 row_ror:8 row_mask:0xf bank_mask:0xf bound_ctrl:1
	v_cndmask_b32_e64 v205, v207, v205, s[4:5]
	v_cndmask_b32_e64 v206, v208, v206, s[4:5]
	v_cmp_eq_u32_e64 s[0:1], 0, v107
	v_add_f32_dpp v205, v205, v205 row_half_mirror row_mask:0xf bank_mask:0xf bound_ctrl:1
	v_add_f32_dpp v206, v206, v206 row_half_mirror row_mask:0xf bank_mask:0xf bound_ctrl:1
	v_cndmask_b32_e64 v205, v206, v205, s[2:3]
	s_nop 1
	v_add_f32_dpp v205, v205, v205 quad_perm:[2,3,0,1] row_mask:0xf bank_mask:0xf bound_ctrl:1
	s_nop 1
	v_add_f32_dpp v205, v205, v205 quad_perm:[1,0,3,2] row_mask:0xf bank_mask:0xf bound_ctrl:1
	v_cndmask_b32_e64 v205, v250, v205, s[0:1]
	s_and_saveexec_b64 s[0:1], vcc
	ds_write_b32 v251, v205
	s_or_b64 exec, exec, s[0:1]
	v_mov_b32_dpp v221, v205 row_ror:8 row_mask:0xf bank_mask:0xf bound_ctrl:1
	v_add_u32_e32 v251, 32, v251
	v_max_f32_e32 v221, v205, v221
	v_mov_b32_e32 v222, v221
	s_nop 1
	v_permlane16_swap_b32_e32 v221, v222
	s_nop 0
	v_max_f32_e32 v221, v221, v222
	v_mov_b32_e32 v222, v221
	s_nop 1
	v_permlane32_swap_b32_e32 v221, v222
	s_nop 0
	v_max3_f32 v223, v248, v221, v222
	v_sub_f32_e32 v224, v248, v223
	v_sub_f32_e32 v225, v205, v223
	v_exp_f32_e32 v224, v224
	v_exp_f32_e32 v225, v225
	v_mov_b32_e32 v248, v223
	s_nop 1
	v_fma_f32 v249, v249, v224, v225
	s_nop 0
	v_readlane_b32 s34, v224, 0
	v_readlane_b32 s36, v224, 4
	v_readlane_b32 s38, v225, 0
	v_readlane_b32 s40, v225, 4
	v_readlane_b32 s42, v225, 8
	v_readlane_b32 s44, v225, 12
	v_readlane_b32 s46, v225, 16
	v_readlane_b32 s48, v225, 20
	v_readlane_b32 s50, v225, 24
	v_readlane_b32 s52, v225, 28
	v_readlane_b32 s54, v225, 32
	v_readlane_b32 s56, v225, 36
	v_readlane_b32 s58, v225, 40
	v_readlane_b32 s60, v225, 44
	v_readlane_b32 s62, v225, 48
	v_readlane_b32 s64, v225, 52
	v_readlane_b32 s66, v225, 56
	v_readlane_b32 s68, v225, 60
	s_nop 1
	v_pk_mul_f32 v[240:241], v[240:241], s[34:35] op_sel_hi:[1,0]
	v_pk_mul_f32 v[242:243], v[242:243], s[34:35] op_sel_hi:[1,0]
	v_pk_mul_f32 v[244:245], v[244:245], s[36:37] op_sel_hi:[1,0]
	v_pk_mul_f32 v[246:247], v[246:247], s[36:37] op_sel_hi:[1,0]
	v_pk_fma_f32 v[240:241], v[70:71], s[38:39], v[240:241] op_sel_hi:[1,0,1]
	v_pk_fma_f32 v[242:243], v[72:73], s[38:39], v[242:243] op_sel_hi:[1,0,1]
	v_pk_fma_f32 v[244:245], v[70:71], s[40:41], v[244:245] op_sel_hi:[1,0,1]
	v_pk_fma_f32 v[246:247], v[72:73], s[40:41], v[246:247] op_sel_hi:[1,0,1]
	v_pk_fma_f32 v[240:241], v[66:67], s[42:43], v[240:241] op_sel_hi:[1,0,1]
	v_pk_fma_f32 v[242:243], v[68:69], s[42:43], v[242:243] op_sel_hi:[1,0,1]
	v_pk_fma_f32 v[244:245], v[66:67], s[44:45], v[244:245] op_sel_hi:[1,0,1]
	v_pk_fma_f32 v[246:247], v[68:69], s[44:45], v[246:247] op_sel_hi:[1,0,1]
	v_pk_fma_f32 v[240:241], v[62:63], s[46:47], v[240:241] op_sel_hi:[1,0,1]
	v_pk_fma_f32 v[242:243], v[64:65], s[46:47], v[242:243] op_sel_hi:[1,0,1]
	v_pk_fma_f32 v[244:245], v[62:63], s[48:49], v[244:245] op_sel_hi:[1,0,1]
	v_pk_fma_f32 v[246:247], v[64:65], s[48:49], v[246:247] op_sel_hi:[1,0,1]
	v_pk_fma_f32 v[240:241], v[58:59], s[50:51], v[240:241] op_sel_hi:[1,0,1]
	v_pk_fma_f32 v[242:243], v[60:61], s[50:51], v[242:243] op_sel_hi:[1,0,1]
	v_pk_fma_f32 v[244:245], v[58:59], s[52:53], v[244:245] op_sel_hi:[1,0,1]
	v_pk_fma_f32 v[246:247], v[60:61], s[52:53], v[246:247] op_sel_hi:[1,0,1]
	v_pk_fma_f32 v[240:241], v[54:55], s[54:55], v[240:241] op_sel_hi:[1,0,1]
	v_pk_fma_f32 v[242:243], v[56:57], s[54:55], v[242:243] op_sel_hi:[1,0,1]
	v_pk_fma_f32 v[244:245], v[54:55], s[56:57], v[244:245] op_sel_hi:[1,0,1]
	v_pk_fma_f32 v[246:247], v[56:57], s[56:57], v[246:247] op_sel_hi:[1,0,1]
	v_pk_fma_f32 v[240:241], v[46:47], s[58:59], v[240:241] op_sel_hi:[1,0,1]
	v_pk_fma_f32 v[242:243], v[48:49], s[58:59], v[242:243] op_sel_hi:[1,0,1]
	v_pk_fma_f32 v[244:245], v[46:47], s[60:61], v[244:245] op_sel_hi:[1,0,1]
	v_pk_fma_f32 v[246:247], v[48:49], s[60:61], v[246:247] op_sel_hi:[1,0,1]
	v_pk_fma_f32 v[240:241], v[34:35], s[62:63], v[240:241] op_sel_hi:[1,0,1]
	v_pk_fma_f32 v[242:243], v[36:37], s[62:63], v[242:243] op_sel_hi:[1,0,1]
	v_pk_fma_f32 v[244:245], v[34:35], s[64:65], v[244:245] op_sel_hi:[1,0,1]
	v_pk_fma_f32 v[246:247], v[36:37], s[64:65], v[246:247] op_sel_hi:[1,0,1]
	v_pk_fma_f32 v[240:241], v[14:15], s[66:67], v[240:241] op_sel_hi:[1,0,1]
	v_pk_fma_f32 v[242:243], v[16:17], s[66:67], v[242:243] op_sel_hi:[1,0,1]
	v_pk_fma_f32 v[244:245], v[14:15], s[68:69], v[244:245] op_sel_hi:[1,0,1]
	v_pk_fma_f32 v[246:247], v[16:17], s[68:69], v[246:247] op_sel_hi:[1,0,1]
	s_cmp_gt_u32 s30, 20
	s_cbranch_scc1 .Lring_noload_0
	global_load_dword v107, v[254:255], off nt
	global_load_dwordx4 v[70:73], v[252:253], off nt
	global_load_dwordx4 v[66:69], v[252:253], off offset:512 nt
	global_load_dwordx4 v[62:65], v[252:253], off offset:1024 nt
	global_load_dwordx4 v[58:61], v[252:253], off offset:1536 nt
	global_load_dwordx4 v[54:57], v[252:253], off offset:2048 nt
	global_load_dwordx4 v[46:49], v[252:253], off offset:2560 nt
	global_load_dwordx4 v[34:37], v[252:253], off offset:3072 nt
	global_load_dwordx4 v[14:17], v[252:253], off offset:3584 nt
	v_lshl_add_u64 v[252:253], v[252:253], 0, s[16:17]
	v_lshl_add_u64 v[254:255], v[254:255], 0, 32
.Lring_noload_0:
	s_add_i32 s30, s30, 1
	s_cmp_eq_u32 s30, 25
	s_cbranch_scc1 .Lring_done

.Lring_go_1:
	v_mul_f32_e32 v205, v10, v102
	v_mul_f32_e32 v206, v6, v102
	v_mul_f32_e32 v207, v10, v98
	v_mul_f32_e32 v208, v6, v98
	v_mul_f32_e32 v209, v10, v94
	v_mul_f32_e32 v210, v6, v94
	v_mul_f32_e32 v211, v10, v90
	v_mul_f32_e32 v212, v6, v90
	v_mul_f32_e32 v213, v10, v86
	v_mul_f32_e32 v214, v6, v86
	v_mul_f32_e32 v215, v10, v82
	v_mul_f32_e32 v216, v6, v82
	v_mul_f32_e32 v217, v10, v78
	v_mul_f32_e32 v218, v6, v78
	v_mul_f32_e32 v219, v10, v74
	v_mul_f32_e32 v220, v6, v74
	v_fmac_f32_e32 v205, v103, v11
	v_fmac_f32_e32 v206, v103, v7
	v_fmac_f32_e32 v207, v99, v11
	v_fmac_f32_e32 v208, v99, v7
	v_fmac_f32_e32 v209, v95, v11
	v_fmac_f32_e32 v210, v95, v7
	v_fmac_f32_e32 v211, v91, v11
	v_fmac_f32_e32 v212, v91, v7
	v_fmac_f32_e32 v213, v87, v11
	v_fmac_f32_e32 v214, v87, v7
	v_fmac_f32_e32 v215, v83, v11
	v_fmac_f32_e32 v216, v83, v7
	v_fmac_f32_e32 v217, v79, v11
	v_fmac_f32_e32 v218, v79, v7
	v_fmac_f32_e32 v219, v75, v11
	v_fmac_f32_e32 v220, v75, v7
	v_fmac_f32_e32 v205, v104, v12
	v_fmac_f32_e32 v206, v104, v8
	v_fmac_f32_e32 v207, v100, v12
	v_fmac_f32_e32 v208, v100, v8
	v_fmac_f32_e32 v209, v96, v12
	v_fmac_f32_e32 v210, v96, v8
	v_fmac_f32_e32 v211, v92, v12
	v_fmac_f32_e32 v212, v92, v8
	v_fmac_f32_e32 v213, v88, v12
	v_fmac_f32_e32 v214, v88, v8
	v_fmac_f32_e32 v215, v84, v12
	v_fmac_f32_e32 v216, v84, v8
	v_fmac_f32_e32 v217, v80, v12
	v_fmac_f32_e32 v218, v80, v8
	v_fmac_f32_e32 v219, v76, v12
	v_fmac_f32_e32 v220, v76, v8
	v_fmac_f32_e32 v205, v105, v13
	v_fmac_f32_e32 v206, v105, v9
	v_fmac_f32_e32 v207, v101, v13
	v_fmac_f32_e32 v208, v101, v9
	v_fmac_f32_e32 v209, v97, v13
	v_fmac_f32_e32 v210, v97, v9
	v_fmac_f32_e32 v211, v93, v13
	v_fmac_f32_e32 v212, v93, v9
	v_fmac_f32_e32 v213, v89, v13
	v_fmac_f32_e32 v214, v89, v9
	v_fmac_f32_e32 v215, v85, v13
	v_fmac_f32_e32 v216, v85, v9
	v_fmac_f32_e32 v217, v81, v13
	v_fmac_f32_e32 v218, v81, v9
	v_fmac_f32_e32 v219, v77, v13
	v_fmac_f32_e32 v220, v77, v9
	v_permlane32_swap_b32_e32 v205, v213
	v_permlane32_swap_b32_e32 v206, v214
	v_permlane32_swap_b32_e32 v207, v215
	v_permlane32_swap_b32_e32 v208, v216
	v_permlane32_swap_b32_e32 v209, v217
	v_permlane32_swap_b32_e32 v210, v218
	v_permlane32_swap_b32_e32 v211, v219
	v_permlane32_swap_b32_e32 v212, v220
	v_add_f32_e32 v205, v205, v213
	v_add_f32_e32 v206, v206, v214
	v_add_f32_e32 v207, v207, v215
	v_add_f32_e32 v208, v208, v216
	v_add_f32_e32 v209, v209, v217
	v_add_f32_e32 v210, v210, v218
	v_add_f32_e32 v211, v211, v219
	v_add_f32_e32 v212, v212, v220
	v_permlane16_swap_b32_e32 v205, v209
	v_permlane16_swap_b32_e32 v206, v210
	v_permlane16_swap_b32_e32 v207, v211
	v_permlane16_swap_b32_e32 v208, v212
	v_add_f32_e32 v205, v205, v209
	v_add_f32_e32 v206, v206, v210
	v_add_f32_e32 v207, v207, v211
	v_add_f32_e32 v208, v208, v212
	v_add_f32_dpp v205, v205, v205 row_ror:8 row_mask:0xf bank_mask:0xf bound_ctrl:1
	v_add_f32_dpp v207, v207, v207 row_ror:8 row_mask:0xf bank_mask:0xf bound_ctrl:1
	v_add_f32_dpp v206, v206, v206 row_ror:8 row_mask:0xf bank_mask:0xf bound_ctrl:1
	v_add_f32_dpp v208, v208, v208 row_ror:8 row_mask:0xf bank_mask:0xf bound_ctrl:1
	v_cndmask_b32_e64 v205, v207, v205, s[4:5]
	v_cndmask_b32_e64 v206, v208, v206, s[4:5]
	v_cmp_eq_u32_e64 s[0:1], 0, v110
	v_add_f32_dpp v205, v205, v205 row_half_mirror row_mask:0xf bank_mask:0xf bound_ctrl:1
	v_add_f32_dpp v206, v206, v206 row_half_mirror row_mask:0xf bank_mask:0xf bound_ctrl:1
	v_cndmask_b32_e64 v205, v206, v205, s[2:3]
	s_nop 1
	v_add_f32_dpp v205, v205, v205 quad_perm:[2,3,0,1] row_mask:0xf bank_mask:0xf bound_ctrl:1
	s_nop 1
	v_add_f32_dpp v205, v205, v205 quad_perm:[1,0,3,2] row_mask:0xf bank_mask:0xf bound_ctrl:1
	v_cndmask_b32_e64 v205, v250, v205, s[0:1]
	s_and_saveexec_b64 s[0:1], vcc
	ds_write_b32 v251, v205
	s_or_b64 exec, exec, s[0:1]
	v_mov_b32_dpp v221, v205 row_ror:8 row_mask:0xf bank_mask:0xf bound_ctrl:1
	v_add_u32_e32 v251, 32, v251
	v_max_f32_e32 v221, v205, v221
	v_mov_b32_e32 v222, v221
	s_nop 1
	v_permlane16_swap_b32_e32 v221, v222
	s_nop 0
	v_max_f32_e32 v221, v221, v222
	v_mov_b32_e32 v222, v221
	s_nop 1
	v_permlane32_swap_b32_e32 v221, v222
	s_nop 0
	v_max3_f32 v223, v248, v221, v222
	v_sub_f32_e32 v224, v248, v223
	v_sub_f32_e32 v225, v205, v223
	v_exp_f32_e32 v224, v224
	v_exp_f32_e32 v225, v225
	v_mov_b32_e32 v248, v223
	s_nop 1
	v_fma_f32 v249, v249, v224, v225
	s_nop 0
	v_readlane_b32 s34, v224, 0
	v_readlane_b32 s36, v224, 4
	v_readlane_b32 s38, v225, 0
	v_readlane_b32 s40, v225, 4
	v_readlane_b32 s42, v225, 8
	v_readlane_b32 s44, v225, 12
	v_readlane_b32 s46, v225, 16
	v_readlane_b32 s48, v225, 20
	v_readlane_b32 s50, v225, 24
	v_readlane_b32 s52, v225, 28
	v_readlane_b32 s54, v225, 32
	v_readlane_b32 s56, v225, 36
	v_readlane_b32 s58, v225, 40
	v_readlane_b32 s60, v225, 44
	v_readlane_b32 s62, v225, 48
	v_readlane_b32 s64, v225, 52
	v_readlane_b32 s66, v225, 56
	v_readlane_b32 s68, v225, 60
	s_nop 1
	v_pk_mul_f32 v[240:241], v[240:241], s[34:35] op_sel_hi:[1,0]
	v_pk_mul_f32 v[242:243], v[242:243], s[34:35] op_sel_hi:[1,0]
	v_pk_mul_f32 v[244:245], v[244:245], s[36:37] op_sel_hi:[1,0]
	v_pk_mul_f32 v[246:247], v[246:247], s[36:37] op_sel_hi:[1,0]
	v_pk_fma_f32 v[240:241], v[102:103], s[38:39], v[240:241] op_sel_hi:[1,0,1]
	v_pk_fma_f32 v[242:243], v[104:105], s[38:39], v[242:243] op_sel_hi:[1,0,1]
	v_pk_fma_f32 v[244:245], v[102:103], s[40:41], v[244:245] op_sel_hi:[1,0,1]
	v_pk_fma_f32 v[246:247], v[104:105], s[40:41], v[246:247] op_sel_hi:[1,0,1]
	v_pk_fma_f32 v[240:241], v[98:99], s[42:43], v[240:241] op_sel_hi:[1,0,1]
	v_pk_fma_f32 v[242:243], v[100:101], s[42:43], v[242:243] op_sel_hi:[1,0,1]
	v_pk_fma_f32 v[244:245], v[98:99], s[44:45], v[244:245] op_sel_hi:[1,0,1]
	v_pk_fma_f32 v[246:247], v[100:101], s[44:45], v[246:247] op_sel_hi:[1,0,1]
	v_pk_fma_f32 v[240:241], v[94:95], s[46:47], v[240:241] op_sel_hi:[1,0,1]
	v_pk_fma_f32 v[242:243], v[96:97], s[46:47], v[242:243] op_sel_hi:[1,0,1]
	v_pk_fma_f32 v[244:245], v[94:95], s[48:49], v[244:245] op_sel_hi:[1,0,1]
	v_pk_fma_f32 v[246:247], v[96:97], s[48:49], v[246:247] op_sel_hi:[1,0,1]
	v_pk_fma_f32 v[240:241], v[90:91], s[50:51], v[240:241] op_sel_hi:[1,0,1]
	v_pk_fma_f32 v[242:243], v[92:93], s[50:51], v[242:243] op_sel_hi:[1,0,1]
	v_pk_fma_f32 v[244:245], v[90:91], s[52:53], v[244:245] op_sel_hi:[1,0,1]
	v_pk_fma_f32 v[246:247], v[92:93], s[52:53], v[246:247] op_sel_hi:[1,0,1]
	v_pk_fma_f32 v[240:241], v[86:87], s[54:55], v[240:241] op_sel_hi:[1,0,1]
	v_pk_fma_f32 v[242:243], v[88:89], s[54:55], v[242:243] op_sel_hi:[1,0,1]
	v_pk_fma_f32 v[244:245], v[86:87], s[56:57], v[244:245] op_sel_hi:[1,0,1]
	v_pk_fma_f32 v[246:247], v[88:89], s[56:57], v[246:247] op_sel_hi:[1,0,1]
	v_pk_fma_f32 v[240:241], v[82:83], s[58:59], v[240:241] op_sel_hi:[1,0,1]
	v_pk_fma_f32 v[242:243], v[84:85], s[58:59], v[242:243] op_sel_hi:[1,0,1]
	v_pk_fma_f32 v[244:245], v[82:83], s[60:61], v[244:245] op_sel_hi:[1,0,1]
	v_pk_fma_f32 v[246:247], v[84:85], s[60:61], v[246:247] op_sel_hi:[1,0,1]
	v_pk_fma_f32 v[240:241], v[78:79], s[62:63], v[240:241] op_sel_hi:[1,0,1]
	v_pk_fma_f32 v[242:243], v[80:81], s[62:63], v[242:243] op_sel_hi:[1,0,1]
	v_pk_fma_f32 v[244:245], v[78:79], s[64:65], v[244:245] op_sel_hi:[1,0,1]
	v_pk_fma_f32 v[246:247], v[80:81], s[64:65], v[246:247] op_sel_hi:[1,0,1]
	v_pk_fma_f32 v[240:241], v[74:75], s[66:67], v[240:241] op_sel_hi:[1,0,1]
	v_pk_fma_f32 v[242:243], v[76:77], s[66:67], v[242:243] op_sel_hi:[1,0,1]
	v_pk_fma_f32 v[244:245], v[74:75], s[68:69], v[244:245] op_sel_hi:[1,0,1]
	v_pk_fma_f32 v[246:247], v[76:77], s[68:69], v[246:247] op_sel_hi:[1,0,1]
	s_cmp_gt_u32 s30, 20
	s_cbranch_scc1 .Lring_noload_1
	global_load_dword v110, v[254:255], off nt
	global_load_dwordx4 v[102:105], v[252:253], off nt
	global_load_dwordx4 v[98:101], v[252:253], off offset:512 nt
	global_load_dwordx4 v[94:97], v[252:253], off offset:1024 nt
	global_load_dwordx4 v[90:93], v[252:253], off offset:1536 nt
	global_load_dwordx4 v[86:89], v[252:253], off offset:2048 nt
	global_load_dwordx4 v[82:85], v[252:253], off offset:2560 nt
	global_load_dwordx4 v[78:81], v[252:253], off offset:3072 nt
	global_load_dwordx4 v[74:77], v[252:253], off offset:3584 nt
	v_lshl_add_u64 v[252:253], v[252:253], 0, s[16:17]
	v_lshl_add_u64 v[254:255], v[254:255], 0, 32
.Lring_noload_1:
	s_add_i32 s30, s30, 1

.Lring_go_2:
	v_mul_f32_e32 v205, v10, v50
	v_mul_f32_e32 v206, v6, v50
	v_mul_f32_e32 v207, v10, v42
	v_mul_f32_e32 v208, v6, v42
	v_mul_f32_e32 v209, v10, v38
	v_mul_f32_e32 v210, v6, v38
	v_mul_f32_e32 v211, v10, v30
	v_mul_f32_e32 v212, v6, v30
	v_mul_f32_e32 v213, v10, v26
	v_mul_f32_e32 v214, v6, v26
	v_mul_f32_e32 v215, v10, v22
	v_mul_f32_e32 v216, v6, v22
	v_mul_f32_e32 v217, v10, v18
	v_mul_f32_e32 v218, v6, v18
	v_mul_f32_e32 v219, v10, v2
	v_mul_f32_e32 v220, v6, v2
	v_fmac_f32_e32 v205, v51, v11
	v_fmac_f32_e32 v206, v51, v7
	v_fmac_f32_e32 v207, v43, v11
	v_fmac_f32_e32 v208, v43, v7
	v_fmac_f32_e32 v209, v39, v11
	v_fmac_f32_e32 v210, v39, v7
	v_fmac_f32_e32 v211, v31, v11
	v_fmac_f32_e32 v212, v31, v7
	v_fmac_f32_e32 v213, v27, v11
	v_fmac_f32_e32 v214, v27, v7
	v_fmac_f32_e32 v215, v23, v11
	v_fmac_f32_e32 v216, v23, v7
	v_fmac_f32_e32 v217, v19, v11
	v_fmac_f32_e32 v218, v19, v7
	v_fmac_f32_e32 v219, v3, v11
	v_fmac_f32_e32 v220, v3, v7
	v_fmac_f32_e32 v205, v52, v12
	v_fmac_f32_e32 v206, v52, v8
	v_fmac_f32_e32 v207, v44, v12
	v_fmac_f32_e32 v208, v44, v8
	v_fmac_f32_e32 v209, v40, v12
	v_fmac_f32_e32 v210, v40, v8
	v_fmac_f32_e32 v211, v32, v12
	v_fmac_f32_e32 v212, v32, v8
	v_fmac_f32_e32 v213, v28, v12
	v_fmac_f32_e32 v214, v28, v8
	v_fmac_f32_e32 v215, v24, v12
	v_fmac_f32_e32 v216, v24, v8
	v_fmac_f32_e32 v217, v20, v12
	v_fmac_f32_e32 v218, v20, v8
	v_fmac_f32_e32 v219, v4, v12
	v_fmac_f32_e32 v220, v4, v8
	v_fmac_f32_e32 v205, v53, v13
	v_fmac_f32_e32 v206, v53, v9
	v_fmac_f32_e32 v207, v45, v13
	v_fmac_f32_e32 v208, v45, v9
	v_fmac_f32_e32 v209, v41, v13
	v_fmac_f32_e32 v210, v41, v9
	v_fmac_f32_e32 v211, v33, v13
	v_fmac_f32_e32 v212, v33, v9
	v_fmac_f32_e32 v213, v29, v13
	v_fmac_f32_e32 v214, v29, v9
	v_fmac_f32_e32 v215, v25, v13
	v_fmac_f32_e32 v216, v25, v9
	v_fmac_f32_e32 v217, v21, v13
	v_fmac_f32_e32 v218, v21, v9
	v_fmac_f32_e32 v219, v5, v13
	v_fmac_f32_e32 v220, v5, v9
	v_permlane32_swap_b32_e32 v205, v213
	v_permlane32_swap_b32_e32 v206, v214
	v_permlane32_swap_b32_e32 v207, v215
	v_permlane32_swap_b32_e32 v208, v216
	v_permlane32_swap_b32_e32 v209, v217
	v_permlane32_swap_b32_e32 v210, v218
	v_permlane32_swap_b32_e32 v211, v219
	v_permlane32_swap_b32_e32 v212, v220
	v_add_f32_e32 v205, v205, v213
	v_add_f32_e32 v206, v206, v214
	v_add_f32_e32 v207, v207, v215
	v_add_f32_e32 v208, v208, v216
	v_add_f32_e32 v209, v209, v217
	v_add_f32_e32 v210, v210, v218
	v_add_f32_e32 v211, v211, v219
	v_add_f32_e32 v212, v212, v220
	v_permlane16_swap_b32_e32 v205, v209
	v_permlane16_swap_b32_e32 v206, v210
	v_permlane16_swap_b32_e32 v207, v211
	v_permlane16_swap_b32_e32 v208, v212
	v_add_f32_e32 v205, v205, v209
	v_add_f32_e32 v206, v206, v210
	v_add_f32_e32 v207, v207, v211
	v_add_f32_e32 v208, v208, v212
	v_add_f32_dpp v205, v205, v205 row_ror:8 row_mask:0xf bank_mask:0xf bound_ctrl:1
	v_add_f32_dpp v207, v207, v207 row_ror:8 row_mask:0xf bank_mask:0xf bound_ctrl:1
	v_add_f32_dpp v206, v206, v206 row_ror:8 row_mask:0xf bank_mask:0xf bound_ctrl:1
	v_add_f32_dpp v208, v208, v208 row_ror:8 row_mask:0xf bank_mask:0xf bound_ctrl:1
	v_cndmask_b32_e64 v205, v207, v205, s[4:5]
	v_cndmask_b32_e64 v206, v208, v206, s[4:5]
	v_cmp_eq_u32_e64 s[0:1], 0, v111
	v_add_f32_dpp v205, v205, v205 row_half_mirror row_mask:0xf bank_mask:0xf bound_ctrl:1
	v_add_f32_dpp v206, v206, v206 row_half_mirror row_mask:0xf bank_mask:0xf bound_ctrl:1
	v_cndmask_b32_e64 v205, v206, v205, s[2:3]
	s_nop 1
	v_add_f32_dpp v205, v205, v205 quad_perm:[2,3,0,1] row_mask:0xf bank_mask:0xf bound_ctrl:1
	s_nop 1
	v_add_f32_dpp v205, v205, v205 quad_perm:[1,0,3,2] row_mask:0xf bank_mask:0xf bound_ctrl:1
	v_cndmask_b32_e64 v205, v250, v205, s[0:1]
	s_and_saveexec_b64 s[0:1], vcc
	ds_write_b32 v251, v205
	s_or_b64 exec, exec, s[0:1]
	v_mov_b32_dpp v221, v205 row_ror:8 row_mask:0xf bank_mask:0xf bound_ctrl:1
	v_add_u32_e32 v251, 32, v251
	v_max_f32_e32 v221, v205, v221
	v_mov_b32_e32 v222, v221
	s_nop 1
	v_permlane16_swap_b32_e32 v221, v222
	s_nop 0
	v_max_f32_e32 v221, v221, v222
	v_mov_b32_e32 v222, v221
	s_nop 1
	v_permlane32_swap_b32_e32 v221, v222
	s_nop 0
	v_max3_f32 v223, v248, v221, v222
	v_sub_f32_e32 v224, v248, v223
	v_sub_f32_e32 v225, v205, v223
	v_exp_f32_e32 v224, v224
	v_exp_f32_e32 v225, v225
	v_mov_b32_e32 v248, v223
	s_nop 1
	v_fma_f32 v249, v249, v224, v225
	s_nop 0
	v_readlane_b32 s34, v224, 0
	v_readlane_b32 s36, v224, 4
	v_readlane_b32 s38, v225, 0
	v_readlane_b32 s40, v225, 4
	v_readlane_b32 s42, v225, 8
	v_readlane_b32 s44, v225, 12
	v_readlane_b32 s46, v225, 16
	v_readlane_b32 s48, v225, 20
	v_readlane_b32 s50, v225, 24
	v_readlane_b32 s52, v225, 28
	v_readlane_b32 s54, v225, 32
	v_readlane_b32 s56, v225, 36
	v_readlane_b32 s58, v225, 40
	v_readlane_b32 s60, v225, 44
	v_readlane_b32 s62, v225, 48
	v_readlane_b32 s64, v225, 52
	v_readlane_b32 s66, v225, 56
	v_readlane_b32 s68, v225, 60
	s_nop 1
	v_pk_mul_f32 v[240:241], v[240:241], s[34:35] op_sel_hi:[1,0]
	v_pk_mul_f32 v[242:243], v[242:243], s[34:35] op_sel_hi:[1,0]
	v_pk_mul_f32 v[244:245], v[244:245], s[36:37] op_sel_hi:[1,0]
	v_pk_mul_f32 v[246:247], v[246:247], s[36:37] op_sel_hi:[1,0]
	v_pk_fma_f32 v[240:241], v[50:51], s[38:39], v[240:241] op_sel_hi:[1,0,1]
	v_pk_fma_f32 v[242:243], v[52:53], s[38:39], v[242:243] op_sel_hi:[1,0,1]
	v_pk_fma_f32 v[244:245], v[50:51], s[40:41], v[244:245] op_sel_hi:[1,0,1]
	v_pk_fma_f32 v[246:247], v[52:53], s[40:41], v[246:247] op_sel_hi:[1,0,1]
	v_pk_fma_f32 v[240:241], v[42:43], s[42:43], v[240:241] op_sel_hi:[1,0,1]
	v_pk_fma_f32 v[242:243], v[44:45], s[42:43], v[242:243] op_sel_hi:[1,0,1]
	v_pk_fma_f32 v[244:245], v[42:43], s[44:45], v[244:245] op_sel_hi:[1,0,1]
	v_pk_fma_f32 v[246:247], v[44:45], s[44:45], v[246:247] op_sel_hi:[1,0,1]
	v_pk_fma_f32 v[240:241], v[38:39], s[46:47], v[240:241] op_sel_hi:[1,0,1]
	v_pk_fma_f32 v[242:243], v[40:41], s[46:47], v[242:243] op_sel_hi:[1,0,1]
	v_pk_fma_f32 v[244:245], v[38:39], s[48:49], v[244:245] op_sel_hi:[1,0,1]
	v_pk_fma_f32 v[246:247], v[40:41], s[48:49], v[246:247] op_sel_hi:[1,0,1]
	v_pk_fma_f32 v[240:241], v[30:31], s[50:51], v[240:241] op_sel_hi:[1,0,1]
	v_pk_fma_f32 v[242:243], v[32:33], s[50:51], v[242:243] op_sel_hi:[1,0,1]
	v_pk_fma_f32 v[244:245], v[30:31], s[52:53], v[244:245] op_sel_hi:[1,0,1]
	v_pk_fma_f32 v[246:247], v[32:33], s[52:53], v[246:247] op_sel_hi:[1,0,1]
	v_pk_fma_f32 v[240:241], v[26:27], s[54:55], v[240:241] op_sel_hi:[1,0,1]
	v_pk_fma_f32 v[242:243], v[28:29], s[54:55], v[242:243] op_sel_hi:[1,0,1]
	v_pk_fma_f32 v[244:245], v[26:27], s[56:57], v[244:245] op_sel_hi:[1,0,1]
	v_pk_fma_f32 v[246:247], v[28:29], s[56:57], v[246:247] op_sel_hi:[1,0,1]
	v_pk_fma_f32 v[240:241], v[22:23], s[58:59], v[240:241] op_sel_hi:[1,0,1]
	v_pk_fma_f32 v[242:243], v[24:25], s[58:59], v[242:243] op_sel_hi:[1,0,1]
	v_pk_fma_f32 v[244:245], v[22:23], s[60:61], v[244:245] op_sel_hi:[1,0,1]
	v_pk_fma_f32 v[246:247], v[24:25], s[60:61], v[246:247] op_sel_hi:[1,0,1]
	v_pk_fma_f32 v[240:241], v[18:19], s[62:63], v[240:241] op_sel_hi:[1,0,1]
	v_pk_fma_f32 v[242:243], v[20:21], s[62:63], v[242:243] op_sel_hi:[1,0,1]
	v_pk_fma_f32 v[244:245], v[18:19], s[64:65], v[244:245] op_sel_hi:[1,0,1]
	v_pk_fma_f32 v[246:247], v[20:21], s[64:65], v[246:247] op_sel_hi:[1,0,1]
	v_pk_fma_f32 v[240:241], v[2:3], s[66:67], v[240:241] op_sel_hi:[1,0,1]
	v_pk_fma_f32 v[242:243], v[4:5], s[66:67], v[242:243] op_sel_hi:[1,0,1]
	v_pk_fma_f32 v[244:245], v[2:3], s[68:69], v[244:245] op_sel_hi:[1,0,1]
	v_pk_fma_f32 v[246:247], v[4:5], s[68:69], v[246:247] op_sel_hi:[1,0,1]
	s_cmp_gt_u32 s30, 20
	s_cbranch_scc1 .Lring_noload_2
	global_load_dword v111, v[254:255], off nt
	global_load_dwordx4 v[50:53], v[252:253], off nt
	global_load_dwordx4 v[42:45], v[252:253], off offset:512 nt
	global_load_dwordx4 v[38:41], v[252:253], off offset:1024 nt
	global_load_dwordx4 v[30:33], v[252:253], off offset:1536 nt
	global_load_dwordx4 v[26:29], v[252:253], off offset:2048 nt
	global_load_dwordx4 v[22:25], v[252:253], off offset:2560 nt
	global_load_dwordx4 v[18:21], v[252:253], off offset:3072 nt
	global_load_dwordx4 v[2:5], v[252:253], off offset:3584 nt
	v_lshl_add_u64 v[252:253], v[252:253], 0, s[16:17]
	v_lshl_add_u64 v[254:255], v[254:255], 0, 32

.Lring_go_3:
	v_mul_f32_e32 v205, v10, v138
	v_mul_f32_e32 v206, v6, v138
	v_mul_f32_e32 v207, v10, v146
	v_mul_f32_e32 v208, v6, v146
	v_mul_f32_e32 v209, v10, v152
	v_mul_f32_e32 v210, v6, v152
	v_mul_f32_e32 v211, v10, v156
	v_mul_f32_e32 v212, v6, v156
	v_mul_f32_e32 v213, v10, v160
	v_mul_f32_e32 v214, v6, v160
	v_mul_f32_e32 v215, v10, v164
	v_mul_f32_e32 v216, v6, v164
	v_mul_f32_e32 v217, v10, v168
	v_mul_f32_e32 v218, v6, v168
	v_mul_f32_e32 v219, v10, v172
	v_mul_f32_e32 v220, v6, v172
	v_fmac_f32_e32 v205, v139, v11
	v_fmac_f32_e32 v206, v139, v7
	v_fmac_f32_e32 v207, v147, v11
	v_fmac_f32_e32 v208, v147, v7
	v_fmac_f32_e32 v209, v153, v11
	v_fmac_f32_e32 v210, v153, v7
	v_fmac_f32_e32 v211, v157, v11
	v_fmac_f32_e32 v212, v157, v7
	v_fmac_f32_e32 v213, v161, v11
	v_fmac_f32_e32 v214, v161, v7
	v_fmac_f32_e32 v215, v165, v11
	v_fmac_f32_e32 v216, v165, v7
	v_fmac_f32_e32 v217, v169, v11
	v_fmac_f32_e32 v218, v169, v7
	v_fmac_f32_e32 v219, v173, v11
	v_fmac_f32_e32 v220, v173, v7
	v_fmac_f32_e32 v205, v140, v12
	v_fmac_f32_e32 v206, v140, v8
	v_fmac_f32_e32 v207, v148, v12
	v_fmac_f32_e32 v208, v148, v8
	v_fmac_f32_e32 v209, v154, v12
	v_fmac_f32_e32 v210, v154, v8
	v_fmac_f32_e32 v211, v158, v12
	v_fmac_f32_e32 v212, v158, v8
	v_fmac_f32_e32 v213, v162, v12
	v_fmac_f32_e32 v214, v162, v8
	v_fmac_f32_e32 v215, v166, v12
	v_fmac_f32_e32 v216, v166, v8
	v_fmac_f32_e32 v217, v170, v12
	v_fmac_f32_e32 v218, v170, v8
	v_fmac_f32_e32 v219, v174, v12
	v_fmac_f32_e32 v220, v174, v8
	v_fmac_f32_e32 v205, v141, v13
	v_fmac_f32_e32 v206, v141, v9
	v_fmac_f32_e32 v207, v149, v13
	v_fmac_f32_e32 v208, v149, v9
	v_fmac_f32_e32 v209, v155, v13
	v_fmac_f32_e32 v210, v155, v9
	v_fmac_f32_e32 v211, v159, v13
	v_fmac_f32_e32 v212, v159, v9
	v_fmac_f32_e32 v213, v163, v13
	v_fmac_f32_e32 v214, v163, v9
	v_fmac_f32_e32 v215, v167, v13
	v_fmac_f32_e32 v216, v167, v9
	v_fmac_f32_e32 v217, v171, v13
	v_fmac_f32_e32 v218, v171, v9
	v_fmac_f32_e32 v219, v175, v13
	v_fmac_f32_e32 v220, v175, v9
	v_permlane32_swap_b32_e32 v205, v213
	v_permlane32_swap_b32_e32 v206, v214
	v_permlane32_swap_b32_e32 v207, v215
	v_permlane32_swap_b32_e32 v208, v216
	v_permlane32_swap_b32_e32 v209, v217
	v_permlane32_swap_b32_e32 v210, v218
	v_permlane32_swap_b32_e32 v211, v219
	v_permlane32_swap_b32_e32 v212, v220
	v_add_f32_e32 v205, v205, v213
	v_add_f32_e32 v206, v206, v214
	v_add_f32_e32 v207, v207, v215
	v_add_f32_e32 v208, v208, v216
	v_add_f32_e32 v209, v209, v217
	v_add_f32_e32 v210, v210, v218
	v_add_f32_e32 v211, v211, v219
	v_add_f32_e32 v212, v212, v220
	v_permlane16_swap_b32_e32 v205, v209
	v_permlane16_swap_b32_e32 v206, v210
	v_permlane16_swap_b32_e32 v207, v211
	v_permlane16_swap_b32_e32 v208, v212
	v_add_f32_e32 v205, v205, v209
	v_add_f32_e32 v206, v206, v210
	v_add_f32_e32 v207, v207, v211
	v_add_f32_e32 v208, v208, v212
	v_add_f32_dpp v205, v205, v205 row_ror:8 row_mask:0xf bank_mask:0xf bound_ctrl:1
	v_add_f32_dpp v207, v207, v207 row_ror:8 row_mask:0xf bank_mask:0xf bound_ctrl:1
	v_add_f32_dpp v206, v206, v206 row_ror:8 row_mask:0xf bank_mask:0xf bound_ctrl:1
	v_add_f32_dpp v208, v208, v208 row_ror:8 row_mask:0xf bank_mask:0xf bound_ctrl:1
	v_cndmask_b32_e64 v205, v207, v205, s[4:5]
	v_cndmask_b32_e64 v206, v208, v206, s[4:5]
	v_cmp_eq_u32_e64 s[0:1], 0, v112
	v_add_f32_dpp v205, v205, v205 row_half_mirror row_mask:0xf bank_mask:0xf bound_ctrl:1
	v_add_f32_dpp v206, v206, v206 row_half_mirror row_mask:0xf bank_mask:0xf bound_ctrl:1
	v_cndmask_b32_e64 v205, v206, v205, s[2:3]
	s_nop 1
	v_add_f32_dpp v205, v205, v205 quad_perm:[2,3,0,1] row_mask:0xf bank_mask:0xf bound_ctrl:1
	s_nop 1
	v_add_f32_dpp v205, v205, v205 quad_perm:[1,0,3,2] row_mask:0xf bank_mask:0xf bound_ctrl:1
	v_cndmask_b32_e64 v205, v250, v205, s[0:1]
	s_and_saveexec_b64 s[0:1], vcc
	ds_write_b32 v251, v205
	s_or_b64 exec, exec, s[0:1]
	v_mov_b32_dpp v221, v205 row_ror:8 row_mask:0xf bank_mask:0xf bound_ctrl:1
	v_add_u32_e32 v251, 32, v251
	v_max_f32_e32 v221, v205, v221
	v_mov_b32_e32 v222, v221
	s_nop 1
	v_permlane16_swap_b32_e32 v221, v222
	s_nop 0
	v_max_f32_e32 v221, v221, v222
	v_mov_b32_e32 v222, v221
	s_nop 1
	v_permlane32_swap_b32_e32 v221, v222
	s_nop 0
	v_max3_f32 v223, v248, v221, v222
	v_sub_f32_e32 v224, v248, v223
	v_sub_f32_e32 v225, v205, v223
	v_exp_f32_e32 v224, v224
	v_exp_f32_e32 v225, v225
	v_mov_b32_e32 v248, v223
	s_nop 1
	v_fma_f32 v249, v249, v224, v225
	s_nop 0
	v_readlane_b32 s34, v224, 0
	v_readlane_b32 s36, v224, 4
	v_readlane_b32 s38, v225, 0
	v_readlane_b32 s40, v225, 4
	v_readlane_b32 s42, v225, 8
	v_readlane_b32 s44, v225, 12
	v_readlane_b32 s46, v225, 16
	v_readlane_b32 s48, v225, 20
	v_readlane_b32 s50, v225, 24
	v_readlane_b32 s52, v225, 28
	v_readlane_b32 s54, v225, 32
	v_readlane_b32 s56, v225, 36
	v_readlane_b32 s58, v225, 40
	v_readlane_b32 s60, v225, 44
	v_readlane_b32 s62, v225, 48
	v_readlane_b32 s64, v225, 52
	v_readlane_b32 s66, v225, 56
	v_readlane_b32 s68, v225, 60
	s_nop 1
	v_pk_mul_f32 v[240:241], v[240:241], s[34:35] op_sel_hi:[1,0]
	v_pk_mul_f32 v[242:243], v[242:243], s[34:35] op_sel_hi:[1,0]
	v_pk_mul_f32 v[244:245], v[244:245], s[36:37] op_sel_hi:[1,0]
	v_pk_mul_f32 v[246:247], v[246:247], s[36:37] op_sel_hi:[1,0]
	v_pk_fma_f32 v[240:241], v[138:139], s[38:39], v[240:241] op_sel_hi:[1,0,1]
	v_pk_fma_f32 v[242:243], v[140:141], s[38:39], v[242:243] op_sel_hi:[1,0,1]
	v_pk_fma_f32 v[244:245], v[138:139], s[40:41], v[244:245] op_sel_hi:[1,0,1]
	v_pk_fma_f32 v[246:247], v[140:141], s[40:41], v[246:247] op_sel_hi:[1,0,1]
	v_pk_fma_f32 v[240:241], v[146:147], s[42:43], v[240:241] op_sel_hi:[1,0,1]
	v_pk_fma_f32 v[242:243], v[148:149], s[42:43], v[242:243] op_sel_hi:[1,0,1]
	v_pk_fma_f32 v[244:245], v[146:147], s[44:45], v[244:245] op_sel_hi:[1,0,1]
	v_pk_fma_f32 v[246:247], v[148:149], s[44:45], v[246:247] op_sel_hi:[1,0,1]
	v_pk_fma_f32 v[240:241], v[152:153], s[46:47], v[240:241] op_sel_hi:[1,0,1]
	v_pk_fma_f32 v[242:243], v[154:155], s[46:47], v[242:243] op_sel_hi:[1,0,1]
	v_pk_fma_f32 v[244:245], v[152:153], s[48:49], v[244:245] op_sel_hi:[1,0,1]
	v_pk_fma_f32 v[246:247], v[154:155], s[48:49], v[246:247] op_sel_hi:[1,0,1]
	v_pk_fma_f32 v[240:241], v[156:157], s[50:51], v[240:241] op_sel_hi:[1,0,1]
	v_pk_fma_f32 v[242:243], v[158:159], s[50:51], v[242:243] op_sel_hi:[1,0,1]
	v_pk_fma_f32 v[244:245], v[156:157], s[52:53], v[244:245] op_sel_hi:[1,0,1]
	v_pk_fma_f32 v[246:247], v[158:159], s[52:53], v[246:247] op_sel_hi:[1,0,1]
	v_pk_fma_f32 v[240:241], v[160:161], s[54:55], v[240:241] op_sel_hi:[1,0,1]
	v_pk_fma_f32 v[242:243], v[162:163], s[54:55], v[242:243] op_sel_hi:[1,0,1]
	v_pk_fma_f32 v[244:245], v[160:161], s[56:57], v[244:245] op_sel_hi:[1,0,1]
	v_pk_fma_f32 v[246:247], v[162:163], s[56:57], v[246:247] op_sel_hi:[1,0,1]
	v_pk_fma_f32 v[240:241], v[164:165], s[58:59], v[240:241] op_sel_hi:[1,0,1]
	v_pk_fma_f32 v[242:243], v[166:167], s[58:59], v[242:243] op_sel_hi:[1,0,1]
	v_pk_fma_f32 v[244:245], v[164:165], s[60:61], v[244:245] op_sel_hi:[1,0,1]
	v_pk_fma_f32 v[246:247], v[166:167], s[60:61], v[246:247] op_sel_hi:[1,0,1]
	v_pk_fma_f32 v[240:241], v[168:169], s[62:63], v[240:241] op_sel_hi:[1,0,1]
	v_pk_fma_f32 v[242:243], v[170:171], s[62:63], v[242:243] op_sel_hi:[1,0,1]
	v_pk_fma_f32 v[244:245], v[168:169], s[64:65], v[244:245] op_sel_hi:[1,0,1]
	v_pk_fma_f32 v[246:247], v[170:171], s[64:65], v[246:247] op_sel_hi:[1,0,1]
	v_pk_fma_f32 v[240:241], v[172:173], s[66:67], v[240:241] op_sel_hi:[1,0,1]
	v_pk_fma_f32 v[242:243], v[174:175], s[66:67], v[242:243] op_sel_hi:[1,0,1]
	v_pk_fma_f32 v[244:245], v[172:173], s[68:69], v[244:245] op_sel_hi:[1,0,1]
	v_pk_fma_f32 v[246:247], v[174:175], s[68:69], v[246:247] op_sel_hi:[1,0,1]
	s_cmp_gt_u32 s30, 20
	s_cbranch_scc1 .Lring_noload_3
	global_load_dword v112, v[254:255], off nt
	global_load_dwordx4 v[138:141], v[252:253], off nt
	global_load_dwordx4 v[146:149], v[252:253], off offset:512 nt
	global_load_dwordx4 v[152:155], v[252:253], off offset:1024 nt
	global_load_dwordx4 v[156:159], v[252:253], off offset:1536 nt
	global_load_dwordx4 v[160:163], v[252:253], off offset:2048 nt
	global_load_dwordx4 v[164:167], v[252:253], off offset:2560 nt
	global_load_dwordx4 v[168:171], v[252:253], off offset:3072 nt
	global_load_dwordx4 v[172:175], v[252:253], off offset:3584 nt
	v_lshl_add_u64 v[252:253], v[252:253], 0, s[16:17]
	v_lshl_add_u64 v[254:255], v[254:255], 0, 32
.Lring_noload_3:
	s_add_i32 s30, s30, 1
	s_branch .Lring_tile_0
.Lring_done:
	s_movk_i32 s0, 0x640
	v_mov_b32_e32 v14, 0x8200
	v_mad_u32_u24 v205, v197, s0, v14
	v_lshlrev_b32_e32 v10, 4, v106
	v_or_b32_e32 v6, 0x2000, v196
	v_add_lshl_u32 v7, v122, v6, 4
	global_load_dwordx4 v[158:161], v10, s[8:9]
	global_load_dwordx4 v[154:157], v10, s[8:9] offset:1024
	global_load_dwordx4 v[146:149], v10, s[8:9] offset:2048
	global_load_dwordx4 v[138:141], v10, s[8:9] offset:3072
	global_load_dwordx4 v[118:121], v131, s[8:9]
	global_load_dwordx4 v[106:109], v132, s[8:9]
	global_load_dwordx4 v[98:101], v133, s[8:9]
	global_load_dwordx4 v[102:105], v134, s[8:9]
	global_load_dwordx4 v[170:173], v135, s[8:9]
	global_load_dwordx4 v[166:169], v137, s[8:9]
	global_load_dwordx4 v[178:181], v136, s[8:9]
	global_load_dwordx4 v[174:177], v142, s[8:9]
	global_load_dwordx4 v[162:165], v143, s[8:9]
	s_nop 0
	global_load_dwordx4 v[134:137], v144, s[8:9]
	global_load_dwordx4 v[114:117], v145, s[8:9]
	global_load_dwordx4 v[110:113], v150, s[8:9]
	global_load_dwordx4 v[94:97], v7, s[8:9]
	global_load_dwordx4 v[90:93], v7, s[8:9] offset:1024
	global_load_dwordx4 v[78:81], v7, s[8:9] offset:2048
	global_load_dwordx4 v[74:77], v7, s[8:9] offset:3072
	v_add_lshl_u32 v7, v123, v6, 4
	v_add_lshl_u32 v8, v124, v6, 4
	global_load_dwordx4 v[66:69], v7, s[8:9]
	global_load_dwordx4 v[58:61], v8, s[8:9]
	v_add_lshl_u32 v7, v125, v6, 4
	v_add_lshl_u32 v8, v126, v6, 4
	global_load_dwordx4 v[62:65], v7, s[8:9]
	global_load_dwordx4 v[54:57], v8, s[8:9]
	v_add_lshl_u32 v7, v127, v6, 4
	v_add_lshl_u32 v8, v128, v6, 4
	global_load_dwordx4 v[150:153], v7, s[8:9]
	global_load_dwordx4 v[142:145], v8, s[8:9]
	v_add_lshl_u32 v7, v129, v6, 4
	v_add_lshl_u32 v8, v130, v6, 4
	global_load_dwordx4 v[130:133], v7, s[8:9]
	global_load_dwordx4 v[126:129], v8, s[8:9]
	v_add_lshl_u32 v7, v192, v6, 4
	v_add_lshl_u32 v8, v202, v6, 4
	global_load_dwordx4 v[122:125], v7, s[8:9]
	global_load_dwordx4 v[82:85], v8, s[8:9]
	v_add_lshl_u32 v7, v203, v6, 4
	v_add_lshl_u32 v6, v204, v6, 4
	global_load_dwordx4 v[86:89], v7, s[8:9]
	global_load_dwordx4 v[70:73], v6, s[8:9]
	v_lshlrev_b32_e32 v187, 2, v195
	v_and_or_b32 v190, v187, 4, s31
	v_or_b32_e32 v208, 1, v190
	v_mul_u32_u24_e32 v6, 0x300, v197
	v_ashrrev_i32_e32 v191, 31, v190
	v_ashrrev_i32_e32 v209, 31, v208
	v_or_b32_e32 v6, v196, v6
	v_lshlrev_b64 v[210:211], 9, v[190:191]
	v_lshlrev_b32_e32 v191, 2, v1
	v_lshlrev_b64 v[222:223], 9, v[208:209]
	v_or_b32_e32 v208, 2, v190
	v_mov_b32_e32 v193, 0
	v_lshlrev_b32_e32 v14, 4, v6
	v_lshl_or_b32 v192, v197, 7, v191
	s_movk_i32 s2, 0xfe00
	v_ashrrev_i32_e32 v209, 31, v208
	v_or_b32_e32 v6, 0x40000, v14
	s_movk_i32 s1, 0x100
	v_lshl_add_u64 v[220:221], s[22:23], 0, v[192:193]
	s_mov_b32 s3, -1
	v_lshlrev_b64 v[226:227], 9, v[208:209]
	v_or_b32_e32 v208, 3, v190
	global_load_dwordx4 v[50:53], v6, s[8:9]
	global_load_dwordx4 v[46:49], v6, s[8:9] offset:1024
	global_load_dwordx4 v[42:45], v6, s[8:9] offset:2048
	global_load_dwordx4 v[30:33], v6, s[8:9] offset:3072
	v_add_u32_e32 v6, 0x41000, v14
	v_add_u32_e32 v7, 0x41400, v14
	v_lshl_add_u64 v[212:213], s[20:21], 0, v[192:193]
	v_lshl_add_u64 v[202:203], v[220:221], 0, s[2:3]
	v_cmp_gt_u32_e32 vcc, s1, v0
	v_ashrrev_i32_e32 v209, 31, v208
	s_movk_i32 s2, 0xfe40
	global_load_dwordx4 v[38:41], v6, s[8:9]
	global_load_dwordx4 v[22:25], v7, s[8:9]
	v_add_u32_e32 v6, 0x41800, v14
	v_add_u32_e32 v7, 0x41c00, v14
	v_cndmask_b32_e32 v203, v203, v213, vcc
	v_cndmask_b32_e32 v202, v202, v212, vcc
	v_lshlrev_b64 v[230:231], 9, v[208:209]
	s_mov_b32 s3, -1
	global_load_dwordx4 v[34:37], v6, s[8:9]
	global_load_dwordx4 v[10:13], v7, s[8:9]
	v_add_u32_e32 v6, 0x42000, v14
	v_add_u32_e32 v7, 0x42400, v14
	v_add_u32_e32 v15, 0x42800, v14
	v_add_u32_e32 v18, 0x42c00, v14
	v_lshl_add_u64 v[206:207], v[202:203], 0, v[210:211]
	v_lshl_add_u64 v[224:225], v[202:203], 0, v[222:223]
	v_lshl_add_u64 v[228:229], v[202:203], 0, v[226:227]
	v_lshl_add_u64 v[202:203], v[202:203], 0, v[230:231]
	v_lshl_add_u64 v[212:213], v[212:213], 0, 64
	v_lshl_add_u64 v[220:221], v[220:221], 0, s[2:3]
	global_load_dwordx4 v[26:29], v6, s[8:9]
	s_nop 0
	global_load_dwordx4 v[6:9], v7, s[8:9]
	s_nop 0
	global_load_dwordx4 v[14:17], v15, s[8:9]
	s_nop 0
	global_load_dwordx4 v[18:21], v18, s[8:9]
	s_nop 0
	global_load_dword v208, v[206:207], off
	s_nop 0
	global_load_dword v207, v[224:225], off
	global_load_dword v204, v[228:229], off
	s_nop 0
	global_load_dword v203, v[202:203], off
	s_nop 0
	global_load_dword v206, v192, s[10:11]
	global_load_dword v202, v192, s[10:11] offset:64
	v_cndmask_b32_e32 v213, v221, v213, vcc
	v_cndmask_b32_e32 v212, v220, v212, vcc
	v_lshl_add_u64 v[210:211], v[212:213], 0, v[210:211]
	v_lshl_add_u64 v[220:221], v[212:213], 0, v[222:223]
	v_lshl_add_u64 v[222:223], v[212:213], 0, v[226:227]
	v_lshl_add_u64 v[224:225], v[212:213], 0, v[230:231]
	global_load_dword v212, v[210:211], off
	s_nop 0
	global_load_dword v211, v[220:221], off
	global_load_dword v210, v[222:223], off
	global_load_dword v209, v[224:225], off
	v_lshl_or_b32 v190, v197, 4, v1
	v_lshlrev_b32_e32 v186, 2, v190
	global_load_dword v189, v186, s[24:25]
	global_load_dword v188, v186, s[26:27]
	v_mov_b32_e32 v233, v249
	v_mov_b32_e32 v232, v248
	v_mov_b32_e32 v214, v240
	v_mov_b32_e32 v215, v241
	v_mov_b32_e32 v216, v242
	v_mov_b32_e32 v217, v243
	v_mov_b32_e32 v218, v244
	v_mov_b32_e32 v219, v245
	v_mov_b32_e32 v220, v246
	v_mov_b32_e32 v221, v247
	s_nop 1
	v_add_f32_dpp v2, v233, v233 row_ror:8 row_mask:0xf bank_mask:0xf bound_ctrl:1
	v_mov_b32_e32 v3, v2
	s_nop 1
	v_permlane16_swap_b32_e32 v2, v3
	v_add_f32_e32 v2, v2, v3
	v_mov_b32_e32 v3, v2
	s_nop 1
	v_permlane32_swap_b32_e32 v2, v3
	v_add_f32_e32 v2, v2, v3
	v_readlane_b32 s2, v232, 4
	v_readlane_b32 s4, v2, 4
	v_readlane_b32 s5, v2, 0
	v_readlane_b32 s3, v232, 0
	v_div_scale_f32 v3, s[0:1], s4, s4, 1.0
	v_rcp_f32_e32 v4, v3
	v_lshl_add_u64 v[182:183], v[182:183], 2, s[28:29]
	v_fma_f32 v2, -v3, v4, 1.0
	v_fmac_f32_e32 v4, v2, v4
	v_div_scale_f32 v2, vcc, 1.0, s4, 1.0
	v_mul_f32_e32 v5, v2, v4
	v_fma_f32 v192, -v3, v5, v2
	v_fmac_f32_e32 v5, v192, v4
	v_fma_f32 v2, -v3, v5, v2
	v_div_scale_f32 v3, s[0:1], s5, s5, 1.0
	v_rcp_f32_e32 v192, v3
	v_div_fmas_f32 v2, v2, v4, v5
	v_div_fixup_f32 v2, v2, s4, 1.0
	s_movk_i32 s0, 0xc8
	v_fma_f32 v4, -v3, v192, 1.0
	v_fmac_f32_e32 v192, v4, v192
	v_div_scale_f32 v4, vcc, 1.0, s5, 1.0
	v_mul_f32_e32 v5, v4, v192
	v_fma_f32 v213, -v3, v5, v4
	v_fmac_f32_e32 v5, v213, v192
	v_fma_f32 v3, -v3, v5, v4
	v_div_fmas_f32 v3, v3, v192, v5
	v_div_fixup_f32 v4, v3, s5, 1.0
	v_pk_mul_f32 v[216:217], v[216:217], v[4:5] op_sel_hi:[1,0]
	v_pk_mul_f32 v[214:215], v[214:215], v[4:5] op_sel_hi:[1,0]
	v_cvt_pk_f16_f32 v217, v216, v217
	v_cvt_pk_f16_f32 v216, v214, v215
	v_pk_mul_f32 v[214:215], v[220:221], v[2:3] op_sel_hi:[1,0]
	v_pk_mul_f32 v[218:219], v[218:219], v[2:3] op_sel_hi:[1,0]
	v_add_u32_e32 v3, v205, v184
	ds_read2_b32 v[220:221], v3 offset0:128 offset1:200
	v_cvt_pk_f16_f32 v215, v214, v215
	v_cvt_pk_f16_f32 v214, v218, v219
	ds_read2st64_b32 v[218:219], v3 offset1:1
	v_add_u32_e32 v192, 32, v3
	ds_write2st64_b64 v185, v[216:217], v[214:215] offset1:1
	ds_read2st64_b32 v[214:215], v192 offset0:4 offset1:5
	s_waitcnt lgkmcnt(3)
	v_subrev_f32_e32 v5, s2, v221
	v_exp_f32_e32 v5, v5
	s_waitcnt lgkmcnt(2)
	v_subrev_f32_e32 v185, s3, v218
	v_exp_f32_e32 v185, v185
	s_waitcnt lgkmcnt(0)
	v_subrev_f32_e32 v205, s2, v214
	v_mul_f32_e32 v5, v2, v5
	v_subrev_f32_e32 v192, s3, v219
	v_exp_f32_e32 v205, v205
	v_fmac_f32_e32 v5, v4, v185
	v_mov_b32_e32 v185, v193
	v_exp_f32_e32 v192, v192
	v_lshl_add_u64 v[182:183], v[182:183], 0, v[184:185]
	v_subrev_f32_e32 v185, s2, v215
	v_mul_f32_e32 v5, 0.5, v5
	v_subrev_f32_e32 v184, s3, v220
	v_exp_f32_e32 v185, v185
	global_store_dword v[182:183], v5, off
	v_mul_f32_e32 v5, v2, v205
	v_exp_f32_e32 v184, v184
	v_fmac_f32_e32 v5, v4, v192
	v_mul_f32_e32 v5, 0.5, v5
	global_store_dword v[182:183], v5, off offset:256
	v_mul_f32_e32 v5, v2, v185
	v_fmac_f32_e32 v5, v4, v184
	v_mul_f32_e32 v5, 0.5, v5
	global_store_dword v[182:183], v5, off offset:512
	v_or_b32_e32 v5, 0xc0, v196
	v_cmp_gt_u32_e32 vcc, s0, v5
	s_and_saveexec_b64 s[0:1], vcc
	s_cbranch_execz .LBB1_19
	v_add_u32_e32 v3, 0x300, v3
	ds_read2_b32 v[184:185], v3 offset1:200
	s_waitcnt lgkmcnt(0)
	v_subrev_f32_e32 v3, s3, v184
	v_subrev_f32_e32 v5, s2, v185
	v_exp_f32_e32 v184, v3
	v_exp_f32_e32 v185, v5
	v_mov_b32_e32 v5, v2
	v_pk_mul_f32 v[2:3], v[4:5], v[184:185]
	s_nop 0
	v_add_f32_e32 v2, v2, v3
	v_mul_f32_e32 v2, 0.5, v2
	global_store_dword v[182:183], v2, off offset:768

	.amdhsa_kernel _Z10k_attn_epiILi2EEvPKfS1_PKiPKDF16_S5_PfS1_S1_S5_S1_S1_S1_S1_S1_S6_
		.amdhsa_group_segment_fixed_size 71424
		.amdhsa_private_segment_fixed_size 0
		.amdhsa_kernarg_size 120
		.amdhsa_user_sgpr_count 2
		.amdhsa_user_sgpr_dispatch_ptr 0
		.amdhsa_user_sgpr_queue_ptr 0
		.amdhsa_user_sgpr_kernarg_segment_ptr 1
		.amdhsa_user_sgpr_dispatch_id 0
		.amdhsa_user_sgpr_kernarg_preload_length 0
		.amdhsa_user_sgpr_kernarg_preload_offset 0
		.amdhsa_user_sgpr_private_segment_size 0
		.amdhsa_uses_dynamic_stack 0
		.amdhsa_enable_private_segment 0
		.amdhsa_system_sgpr_workgroup_id_x 1
		.amdhsa_system_sgpr_workgroup_id_y 0
		.amdhsa_system_sgpr_workgroup_id_z 0
		.amdhsa_system_sgpr_workgroup_info 0
		.amdhsa_system_vgpr_workitem_id 0
		.amdhsa_next_free_vgpr 256
		.amdhsa_next_free_sgpr 96
		.amdhsa_accum_offset 256
		.amdhsa_reserve_vcc 1
		.amdhsa_float_round_mode_32 0
		.amdhsa_float_round_mode_16_64 0
		.amdhsa_float_denorm_mode_32 3
		.amdhsa_float_denorm_mode_16_64 3
		.amdhsa_dx10_clamp 1
		.amdhsa_ieee_mode 1
		.amdhsa_fp16_overflow 0
		.amdhsa_tg_split 0
		.amdhsa_exception_fp_ieee_invalid_op 0
		.amdhsa_exception_fp_denorm_src 0
		.amdhsa_exception_fp_ieee_div_zero 0
		.amdhsa_exception_fp_ieee_overflow 0
		.amdhsa_exception_fp_ieee_underflow 0
		.amdhsa_exception_fp_ieee_inexact 0
		.amdhsa_exception_int_div_zero 0
	.end_amdhsa_kernel

amdhsa.kernels:
  - .agpr_count:     0
    .args:
      - .actual_access:  read_only
        .address_space:  global
        .offset:         0
        .size:           8
        .value_kind:     global_buffer
      - .actual_access:  read_only
        .address_space:  global
        .offset:         8
        .size:           8
        .value_kind:     global_buffer
      - .actual_access:  read_only
        .address_space:  global
        .offset:         16
        .size:           8
        .value_kind:     global_buffer
      - .actual_access:  read_only
        .address_space:  global
        .offset:         24
        .size:           8
        .value_kind:     global_buffer
      - .actual_access:  read_only
        .address_space:  global
        .offset:         32
        .size:           8
        .value_kind:     global_buffer
      - .actual_access:  read_only
        .address_space:  global
        .offset:         40
        .size:           8
        .value_kind:     global_buffer
      - .actual_access:  write_only
        .address_space:  global
        .offset:         48
        .size:           8
        .value_kind:     global_buffer
      - .actual_access:  write_only
        .address_space:  global
        .offset:         56
        .size:           8
        .value_kind:     global_buffer
      - .actual_access:  write_only
        .address_space:  global
        .offset:         64
        .size:           8
        .value_kind:     global_buffer
    .group_segment_fixed_size: 0
    .kernarg_segment_align: 8
    .kernarg_segment_size: 72
    .language:       OpenCL C
    .language_version:
      - 2
      - 0
    .max_flat_workgroup_size: 320
    .name:           _Z6k_prepPKfS0_S0_S0_S0_S0_PDF16_S1_S1_
    .private_segment_fixed_size: 0
    .sgpr_count:     20
    .sgpr_spill_count: 0
    .symbol:         _Z6k_prepPKfS0_S0_S0_S0_S0_PDF16_S1_S1_.kd
    .uniform_work_group_size: 1
    .uses_dynamic_stack: false
    .vgpr_count:     16
    .vgpr_spill_count: 0
    .wavefront_size: 64
  - .agpr_count:     0
    .args:
      - .actual_access:  read_only
        .address_space:  global
        .offset:         0
        .size:           8
        .value_kind:     global_buffer
      - .actual_access:  read_only
        .address_space:  global
        .offset:         8
        .size:           8
        .value_kind:     global_buffer
      - .actual_access:  read_only
        .address_space:  global
        .offset:         16
        .size:           8
        .value_kind:     global_buffer
      - .actual_access:  read_only
        .address_space:  global
        .offset:         24
        .size:           8
        .value_kind:     global_buffer
      - .actual_access:  read_only
        .address_space:  global
        .offset:         32
        .size:           8
        .value_kind:     global_buffer
      - .actual_access:  write_only
        .address_space:  global
        .offset:         40
        .size:           8
        .value_kind:     global_buffer
      - .actual_access:  read_only
        .address_space:  global
        .offset:         48
        .size:           8
        .value_kind:     global_buffer
      - .actual_access:  read_only
        .address_space:  global
        .offset:         56
        .size:           8
        .value_kind:     global_buffer
      - .actual_access:  read_only
        .address_space:  global
        .offset:         64
        .size:           8
        .value_kind:     global_buffer
      - .actual_access:  read_only
        .address_space:  global
        .offset:         72
        .size:           8
        .value_kind:     global_buffer
      - .actual_access:  read_only
        .address_space:  global
        .offset:         80
        .size:           8
        .value_kind:     global_buffer
      - .actual_access:  read_only
        .address_space:  global
        .offset:         88
        .size:           8
        .value_kind:     global_buffer
      - .actual_access:  read_only
        .address_space:  global
        .offset:         96
        .size:           8
        .value_kind:     global_buffer
      - .actual_access:  read_only
        .address_space:  global
        .offset:         104
        .size:           8
        .value_kind:     global_buffer
      - .actual_access:  write_only
        .address_space:  global
        .offset:         112
        .size:           8
        .value_kind:     global_buffer
    .group_segment_fixed_size: 71424
    .kernarg_segment_align: 8
    .kernarg_segment_size: 120
    .language:       OpenCL C
    .language_version:
      - 2
      - 0
    .max_flat_workgroup_size: 512
    .name:           _Z10k_attn_epiILi2EEvPKfS1_PKiPKDF16_S5_PfS1_S1_S5_S1_S1_S1_S1_S1_S6_
    .private_segment_fixed_size: 0
    .sgpr_count:     76
    .sgpr_spill_count: 0
    .symbol:         _Z10k_attn_epiILi2EEvPKfS1_PKiPKDF16_S5_PfS1_S1_S5_S1_S1_S1_S1_S1_S6_.kd
    .uniform_work_group_size: 1
    .uses_dynamic_stack: false
    .vgpr_count:     256
    .vgpr_spill_count: 0
    .wavefront_size: 64
